# mixer HGRN2 stage 2: cross-wave prefix as a packed fma chain with scalar 0/1 factors (on top of deferred v-row wait)
# speedup vs baseline: 1.0102x; 1.0012x over previous
.LBB0_472:
	s_mov_b64 s[8:9], -1
	s_and_b64 vcc, exec, s[78:79]
	v_add_u32_e32 v72, 0, v103
	v_add_u32_e32 v153, s1, v108
	s_cbranch_vccnz .LBB0_474
	v_add_u32_e32 v74, 0x1a000, v72
	ds_read2st64_b64 v[160:163], v74 offset1:1
	ds_read2st64_b64 v[164:167], v74 offset0:2 offset1:3
	ds_read2st64_b64 v[168:171], v74 offset0:4 offset1:5
	ds_read2st64_b64 v[172:175], v74 offset0:6 offset1:7
	s_mov_b64 s[8:9], 0
	s_and_b32 s5, s60, 0x3f800000
	s_and_b32 s32, s62, 0x3f800000
	s_and_b32 s40, s64, 0x3f800000
	s_and_b32 s41, s66, 0x3f800000
	s_and_b32 s78, s68, 0x3f800000
	s_and_b32 s79, s70, 0x3f800000
	s_and_b32 s98, s72, 0x3f800000
	s_waitcnt lgkmcnt(0)
	v_pk_fma_f32 v[154:155], v[160:161], s[4:5], 0 op_sel:[0,1,0] op_sel_hi:[1,1,0]
	v_pk_add_f32 v[74:75], v[160:161], 0 op_sel_hi:[1,0]
	v_pk_fma_f32 v[154:155], v[162:163], s[32:33], v[154:155] op_sel:[0,0,0] op_sel_hi:[1,0,1]
	v_pk_add_f32 v[74:75], v[74:75], v[162:163]
	v_pk_fma_f32 v[154:155], v[164:165], s[40:41], v[154:155] op_sel:[0,0,0] op_sel_hi:[1,0,1]
	v_pk_add_f32 v[74:75], v[74:75], v[164:165]
	v_pk_fma_f32 v[154:155], v[166:167], s[40:41], v[154:155] op_sel:[0,1,0] op_sel_hi:[1,1,1]
	v_pk_add_f32 v[160:161], v[74:75], v[166:167]
	v_pk_fma_f32 v[154:155], v[168:169], s[78:79], v[154:155] op_sel:[0,0,0] op_sel_hi:[1,0,1]
	v_pk_fma_f32 v[154:155], v[170:171], s[78:79], v[154:155] op_sel:[0,1,0] op_sel_hi:[1,1,1]
	v_pk_fma_f32 v[154:155], v[172:173], s[98:99], v[154:155] op_sel:[0,0,0] op_sel_hi:[1,0,1]
	v_pk_add_f32 v[74:75], v[160:161], v[168:169]
	v_pk_add_f32 v[220:221], v[220:221], v[154:155] op_sel_hi:[1,0]
	v_pk_add_f32 v[232:233], v[232:233], v[154:155] op_sel:[0,1] op_sel_hi:[1,1]
	v_pk_add_f32 v[222:223], v[222:223], v[154:155] op_sel_hi:[1,0]
	v_pk_add_f32 v[234:235], v[234:235], v[154:155] op_sel:[0,1] op_sel_hi:[1,1]
	v_pk_add_f32 v[224:225], v[224:225], v[154:155] op_sel_hi:[1,0]
	v_pk_add_f32 v[236:237], v[236:237], v[154:155] op_sel:[0,1] op_sel_hi:[1,1]
	v_pk_add_f32 v[226:227], v[226:227], v[154:155] op_sel_hi:[1,0]
	v_pk_add_f32 v[238:239], v[238:239], v[154:155] op_sel:[0,1] op_sel_hi:[1,1]
	v_pk_add_f32 v[74:75], v[74:75], v[170:171]
	v_pk_add_f32 v[220:221], v[220:221], v[160:161] op_sel_hi:[1,0] neg_lo:[0,1] neg_hi:[0,1]
	v_pk_add_f32 v[232:233], v[232:233], v[160:161] op_sel:[0,1] op_sel_hi:[1,1] neg_lo:[0,1] neg_hi:[0,1]
	v_pk_add_f32 v[222:223], v[222:223], v[160:161] op_sel_hi:[1,0] neg_lo:[0,1] neg_hi:[0,1]
	v_pk_add_f32 v[234:235], v[234:235], v[160:161] op_sel:[0,1] op_sel_hi:[1,1] neg_lo:[0,1] neg_hi:[0,1]
	v_pk_add_f32 v[224:225], v[224:225], v[160:161] op_sel_hi:[1,0] neg_lo:[0,1] neg_hi:[0,1]
	v_pk_add_f32 v[236:237], v[236:237], v[160:161] op_sel:[0,1] op_sel_hi:[1,1] neg_lo:[0,1] neg_hi:[0,1]
	v_pk_add_f32 v[226:227], v[226:227], v[160:161] op_sel_hi:[1,0] neg_lo:[0,1] neg_hi:[0,1]
	v_pk_add_f32 v[238:239], v[238:239], v[160:161] op_sel:[0,1] op_sel_hi:[1,1] neg_lo:[0,1] neg_hi:[0,1]
	v_pk_add_f32 v[74:75], v[74:75], v[172:173]
	v_med3_f32 v220, v220, s12, v228
	v_med3_f32 v221, v221, s12, v228
	v_med3_f32 v232, v232, s12, v228
	v_med3_f32 v233, v233, s12, v228
	v_med3_f32 v222, v222, s12, v228
	v_med3_f32 v223, v223, s12, v228
	v_med3_f32 v234, v234, s12, v228
	v_med3_f32 v235, v235, s12, v228
	v_med3_f32 v224, v224, s12, v228
	v_med3_f32 v225, v225, s12, v228
	v_med3_f32 v236, v236, s12, v228
	v_med3_f32 v237, v237, s12, v228
	v_med3_f32 v226, v226, s12, v228
	v_med3_f32 v227, v227, s12, v228
	v_med3_f32 v238, v238, s12, v228
	v_med3_f32 v239, v239, s12, v228
	v_pk_add_f32 v[74:75], v[74:75], v[174:175]
	v_add_u32_e32 v166, 0x4400, v153
	v_add_u32_e32 v167, 0x400, v153
	v_pk_add_f32 v[162:163], v[74:75], v[160:161] neg_lo:[0,1] neg_hi:[0,1]
	v_exp_f32_e32 v220, v220
	v_exp_f32_e32 v221, v221
	v_exp_f32_e32 v232, v232
	v_exp_f32_e32 v233, v233
	v_exp_f32_e32 v222, v222
	v_exp_f32_e32 v223, v223
	v_exp_f32_e32 v234, v234
	v_exp_f32_e32 v235, v235
	v_exp_f32_e32 v224, v224
	v_exp_f32_e32 v225, v225
	v_exp_f32_e32 v236, v236
	v_exp_f32_e32 v237, v237
	v_exp_f32_e32 v226, v226
	v_exp_f32_e32 v227, v227
	v_exp_f32_e32 v238, v238
	v_exp_f32_e32 v239, v239
	v_exp_f32_e32 v156, v162
	v_exp_f32_e32 v157, v163
	v_add_u32_e32 v168, 0x4800, v153
	v_rcp_f32_e32 v176, v220
	v_rcp_f32_e32 v177, v221
	v_rcp_f32_e32 v184, v232
	v_rcp_f32_e32 v185, v233
	v_rcp_f32_e32 v178, v222
	v_rcp_f32_e32 v179, v223
	v_rcp_f32_e32 v186, v234
	v_rcp_f32_e32 v187, v235
	v_rcp_f32_e32 v180, v224
	v_rcp_f32_e32 v181, v225
	v_rcp_f32_e32 v188, v236
	v_rcp_f32_e32 v189, v237
	v_rcp_f32_e32 v182, v226
	v_rcp_f32_e32 v183, v227
	v_rcp_f32_e32 v190, v238
	v_rcp_f32_e32 v191, v239
	v_pk_mul_f32 v[220:221], v[200:201], v[220:221]
	v_pk_mul_f32 v[232:233], v[208:209], v[232:233]
	v_pk_mul_f32 v[222:223], v[202:203], v[222:223]
	v_pk_mul_f32 v[234:235], v[210:211], v[234:235]
	v_pk_mul_f32 v[224:225], v[204:205], v[224:225]
	v_pk_mul_f32 v[236:237], v[212:213], v[236:237]
	v_pk_mul_f32 v[226:227], v[206:207], v[226:227]
	v_pk_mul_f32 v[238:239], v[214:215], v[238:239]
	v_pk_mul_f32 v[78:79], v[176:177], v[156:157] op_sel_hi:[1,0]
	v_pk_mul_f32 v[80:81], v[184:185], v[156:157] op_sel:[0,1] op_sel_hi:[1,1]
	v_pk_mul_f32 v[82:83], v[178:179], v[156:157] op_sel_hi:[1,0]
	v_pk_mul_f32 v[84:85], v[186:187], v[156:157] op_sel:[0,1] op_sel_hi:[1,1]
	v_pk_mul_f32 v[86:87], v[180:181], v[156:157] op_sel_hi:[1,0]
	v_pk_mul_f32 v[88:89], v[188:189], v[156:157] op_sel:[0,1] op_sel_hi:[1,1]
	v_pk_mul_f32 v[90:91], v[182:183], v[156:157] op_sel_hi:[1,0]
	v_pk_mul_f32 v[92:93], v[190:191], v[156:157] op_sel:[0,1] op_sel_hi:[1,1]
	v_pk_mul_f32 v[176:177], v[2:3], v[176:177]
	v_pk_mul_f32 v[184:185], v[10:11], v[184:185]
	v_pk_mul_f32 v[178:179], v[4:5], v[178:179]
	v_pk_mul_f32 v[186:187], v[12:13], v[186:187]
	v_pk_mul_f32 v[180:181], v[6:7], v[180:181]
	v_pk_mul_f32 v[188:189], v[14:15], v[188:189]
	v_pk_mul_f32 v[182:183], v[8:9], v[182:183]
	v_pk_mul_f32 v[190:191], v[16:17], v[190:191]
	v_pk_mul_f32 v[78:79], v[2:3], v[78:79]
	v_pk_mul_f32 v[80:81], v[10:11], v[80:81]
	v_pk_mul_f32 v[82:83], v[4:5], v[82:83]
	v_pk_mul_f32 v[84:85], v[12:13], v[84:85]
	v_pk_mul_f32 v[86:87], v[6:7], v[86:87]
	v_pk_mul_f32 v[88:89], v[14:15], v[88:89]
	v_pk_mul_f32 v[90:91], v[8:9], v[90:91]
	v_pk_mul_f32 v[92:93], v[16:17], v[92:93]
	v_cvt_pk_bf16_f32 v158, v220, v232
	v_cvt_pk_bf16_f32 v159, v221, v233
	v_cvt_pk_bf16_f32 v164, v222, v234
	v_cvt_pk_bf16_f32 v165, v223, v235
	v_cvt_pk_bf16_f32 v169, v224, v236
	v_cvt_pk_bf16_f32 v170, v225, v237
	v_cvt_pk_bf16_f32 v171, v226, v238
	v_cvt_pk_bf16_f32 v172, v227, v239
	ds_write2_b32 v153, v158, v159 offset1:68
	ds_write2_b32 v153, v164, v165 offset0:136 offset1:204
	ds_write2_b32 v167, v169, v170 offset0:16 offset1:84
	ds_write2_b32 v167, v171, v172 offset0:152 offset1:220
	v_cvt_pk_bf16_f32 v173, v176, v184
	v_cvt_pk_bf16_f32 v174, v177, v185
	v_cvt_pk_bf16_f32 v175, v178, v186
	v_cvt_pk_bf16_f32 v162, v179, v187
	v_cvt_pk_bf16_f32 v163, v180, v188
	v_cvt_pk_bf16_f32 v154, v181, v189
	v_cvt_pk_bf16_f32 v155, v182, v190
	v_cvt_pk_bf16_f32 v160, v183, v191
	ds_write2_b32 v166, v173, v174 offset1:68
	ds_write2_b32 v166, v175, v162 offset0:136 offset1:204
	ds_write2_b32 v168, v163, v154 offset0:16 offset1:84
	ds_write2_b32 v168, v155, v160 offset0:152 offset1:220
